# speedup vs baseline: 1.0714x; 1.0090x over previous
.Lm_nok_p2:
	v_add_u32_e32 v128, s46, v2
	v_add_u32_e32 v129, s47, v2
	ds_read_b128 v[88:91], v128 offset:24576
	ds_read_b128 v[92:95], v128 offset:25600
	ds_read_b128 v[96:99], v128 offset:0
	ds_read_b128 v[104:107], v128 offset:2048
	ds_read_b128 v[100:103], v128 offset:1024
	ds_read_b128 v[108:111], v128 offset:3072
	s_waitcnt lgkmcnt(5)
	v_mfma_f32_32x32x16_f16 v[48:63], v[88:91], v[8:11], 0
	s_nop 5
	s_waitcnt lgkmcnt(4)
	v_mfma_f32_32x32x16_f16 v[64:79], v[92:95], v[8:11], 0
	ds_read_b128 v[88:91], v128 offset:26624
	ds_read_b128 v[112:115], v128 offset:4096
	ds_read_b128 v[120:123], v128 offset:6144
	v_exp_f32_e32 v48, v48
	v_exp_f32_e32 v49, v49
	v_exp_f32_e32 v50, v50
	v_exp_f32_e32 v51, v51
	v_exp_f32_e32 v52, v52
	v_exp_f32_e32 v53, v53
	v_exp_f32_e32 v54, v54
	v_exp_f32_e32 v55, v55
	v_cvt_pk_bf16_f32 v80, v48, v49
	v_cvt_pk_bf16_f32 v81, v50, v51
	v_cvt_pk_bf16_f32 v82, v52, v53
	v_cvt_pk_bf16_f32 v83, v54, v55
	ds_read_b128 v[116:119], v128 offset:5120
	ds_read_b128 v[124:127], v128 offset:7168
	v_exp_f32_e32 v56, v56
	v_exp_f32_e32 v57, v57
	v_exp_f32_e32 v58, v58
	v_exp_f32_e32 v59, v59
	s_waitcnt lgkmcnt(7)
	v_mfma_f32_32x32x16_bf16 v[16:31], v[96:99], v[80:83], v[16:31]
	v_exp_f32_e32 v60, v60
	v_exp_f32_e32 v61, v61
	v_exp_f32_e32 v62, v62
	v_exp_f32_e32 v63, v63
	v_mfma_f32_32x32x16_bf16 v[32:47], v[104:107], v[80:83], v[32:47]
	v_cvt_pk_bf16_f32 v84, v56, v57
	v_cvt_pk_bf16_f32 v85, v58, v59
	v_cvt_pk_bf16_f32 v86, v60, v61
	v_cvt_pk_bf16_f32 v87, v62, v63
	s_branch .Lm_steps1
.Lm_steps:
	s_waitcnt lgkmcnt(4)
	v_mfma_f32_32x32x16_f16 v[64:79], v[92:95], v[8:11], 0
	ds_read_b128 v[88:91], v128 offset:26624
	s_sub_u32 s30, s28, s25
	ds_read_b128 v[112:115], v128 offset:4096
	s_mul_i32 s30, s30, 6
	ds_read_b128 v[120:123], v128 offset:6144
	s_add_u32 s30, s30, s24
	v_exp_f32_e32 v48, v48
	s_mul_i32 s31, s28, 6
	v_exp_f32_e32 v49, v49
	s_add_u32 s31, s31, s22
	v_exp_f32_e32 v50, v50
	s_cmp_lt_u32 s28, s25
	v_exp_f32_e32 v51, v51
	s_cselect_b32 s30, s31, s30
	v_exp_f32_e32 v52, v52
	s_lshl_b32 s33, s18, 10
	v_exp_f32_e32 v53, v53
	s_lshl_b32 s31, s30, 12
	v_exp_f32_e32 v54, v54
	s_add_u32 s31, s31, s33
	v_exp_f32_e32 v55, v55
	s_add_u32 s50, s8, s31
	v_cvt_pk_bf16_f32 v80, v48, v49
	s_addc_u32 s51, s9, 0
	v_cvt_pk_bf16_f32 v81, v50, v51
	s_add_u32 s52, s50, 0x3000
	v_cvt_pk_bf16_f32 v82, v52, v53
	s_addc_u32 s53, s51, 0
	v_cvt_pk_bf16_f32 v83, v54, v55
	s_lshl_b32 s31, s30, 10
	ds_read_b128 v[116:119], v128 offset:5120
	s_add_u32 s31, s31, s33
	ds_read_b128 v[124:127], v128 offset:7168
	s_add_u32 s54, s4, s31
	v_exp_f32_e32 v56, v56
	s_addc_u32 s55, s5, 0
	v_exp_f32_e32 v57, v57
	s_add_u32 s34, s48, s33
	v_exp_f32_e32 v58, v58
	s_add_u32 s35, s34, 0x3000
	v_exp_f32_e32 v59, v59
	s_add_u32 s36, s34, 24576
	s_waitcnt lgkmcnt(7)
	v_mfma_f32_32x32x16_bf16 v[16:31], v[96:99], v[80:83], v[16:31]
	v_exp_f32_e32 v60, v60
	v_exp_f32_e32 v61, v61
	v_exp_f32_e32 v62, v62
	v_exp_f32_e32 v63, v63
	v_mfma_f32_32x32x16_bf16 v[32:47], v[104:107], v[80:83], v[32:47]
	v_cvt_pk_bf16_f32 v84, v56, v57
	v_cvt_pk_bf16_f32 v85, v58, v59
	v_cvt_pk_bf16_f32 v86, v60, v61
	v_cvt_pk_bf16_f32 v87, v62, v63
	s_cmp_lt_u32 s28, 9
	s_cbranch_scc0 .Lm_nod_lp
	s_mov_b32 m0, s34
	s_nop 0
	global_load_lds_dwordx4 v2, s[50:51]
	s_mov_b32 m0, s35
	s_nop 0
	global_load_lds_dwordx4 v2, s[52:53]
	s_cmp_lt_u32 s18, 6
	s_cbranch_scc0 .Lm_nod_lp
	s_mov_b32 m0, s36
	s_nop 0
	global_load_lds_dwordx4 v2, s[54:55]
.Lm_nod_lp:
.Lm_steps1:
	s_waitcnt lgkmcnt(4)
	v_mfma_f32_32x32x16_f16 v[48:63], v[88:91], v[8:11], 0
	ds_read_b128 v[92:95], v128 offset:27648
	ds_read_b128 v[96:99], v128 offset:8192
	ds_read_b128 v[104:107], v128 offset:10240
	v_exp_f32_e32 v64, v64
	v_exp_f32_e32 v65, v65
	v_exp_f32_e32 v66, v66
	v_exp_f32_e32 v67, v67
	v_mfma_f32_32x32x16_bf16 v[16:31], v[100:103], v[84:87], v[16:31]
	v_exp_f32_e32 v68, v68
	v_exp_f32_e32 v69, v69
	v_exp_f32_e32 v70, v70
	v_exp_f32_e32 v71, v71
	v_mfma_f32_32x32x16_bf16 v[32:47], v[108:111], v[84:87], v[32:47]
	v_cvt_pk_bf16_f32 v80, v64, v65
	v_cvt_pk_bf16_f32 v81, v66, v67
	v_cvt_pk_bf16_f32 v82, v68, v69
	v_cvt_pk_bf16_f32 v83, v70, v71
	ds_read_b128 v[100:103], v128 offset:9216
	ds_read_b128 v[108:111], v128 offset:11264
	v_exp_f32_e32 v72, v72
	v_exp_f32_e32 v73, v73
	v_exp_f32_e32 v74, v74
	v_exp_f32_e32 v75, v75
	s_waitcnt lgkmcnt(7)
	v_mfma_f32_32x32x16_bf16 v[16:31], v[112:115], v[80:83], v[16:31]
	v_exp_f32_e32 v76, v76
	v_exp_f32_e32 v77, v77
	v_exp_f32_e32 v78, v78
	v_exp_f32_e32 v79, v79
	v_mfma_f32_32x32x16_bf16 v[32:47], v[120:123], v[80:83], v[32:47]
	v_cvt_pk_bf16_f32 v84, v72, v73
	v_cvt_pk_bf16_f32 v85, v74, v75
	v_cvt_pk_bf16_f32 v86, v76, v77
	v_cvt_pk_bf16_f32 v87, v78, v79
	s_waitcnt lgkmcnt(4)
	v_mfma_f32_32x32x16_f16 v[64:79], v[92:95], v[8:11], 0
	ds_read_b128 v[88:91], v128 offset:28672
	ds_read_b128 v[112:115], v128 offset:12288
	ds_read_b128 v[120:123], v128 offset:14336
	v_exp_f32_e32 v48, v48
	v_exp_f32_e32 v49, v49
	v_exp_f32_e32 v50, v50
	v_exp_f32_e32 v51, v51
	v_mfma_f32_32x32x16_bf16 v[16:31], v[116:119], v[84:87], v[16:31]
	v_exp_f32_e32 v52, v52
	v_exp_f32_e32 v53, v53
	v_exp_f32_e32 v54, v54
	v_exp_f32_e32 v55, v55
	v_mfma_f32_32x32x16_bf16 v[32:47], v[124:127], v[84:87], v[32:47]
	v_cvt_pk_bf16_f32 v80, v48, v49
	v_cvt_pk_bf16_f32 v81, v50, v51
	v_cvt_pk_bf16_f32 v82, v52, v53
	v_cvt_pk_bf16_f32 v83, v54, v55
	ds_read_b128 v[116:119], v128 offset:13312
	ds_read_b128 v[124:127], v128 offset:15360
	v_exp_f32_e32 v56, v56
	v_exp_f32_e32 v57, v57
	v_exp_f32_e32 v58, v58
	v_exp_f32_e32 v59, v59
	s_waitcnt lgkmcnt(7)
	v_mfma_f32_32x32x16_bf16 v[16:31], v[96:99], v[80:83], v[16:31]
	v_exp_f32_e32 v60, v60
	v_exp_f32_e32 v61, v61
	v_exp_f32_e32 v62, v62
	v_exp_f32_e32 v63, v63
	v_mfma_f32_32x32x16_bf16 v[32:47], v[104:107], v[80:83], v[32:47]
	v_cvt_pk_bf16_f32 v84, v56, v57
	v_cvt_pk_bf16_f32 v85, v58, v59
	v_cvt_pk_bf16_f32 v86, v60, v61
	v_cvt_pk_bf16_f32 v87, v62, v63
	s_waitcnt lgkmcnt(4)
	v_mfma_f32_32x32x16_f16 v[48:63], v[88:91], v[8:11], 0
	ds_read_b128 v[92:95], v128 offset:29696
	ds_read_b128 v[96:99], v128 offset:16384
	ds_read_b128 v[104:107], v128 offset:18432
	v_exp_f32_e32 v64, v64
	v_exp_f32_e32 v65, v65
	v_exp_f32_e32 v66, v66
	v_exp_f32_e32 v67, v67
	v_mfma_f32_32x32x16_bf16 v[16:31], v[100:103], v[84:87], v[16:31]
	v_exp_f32_e32 v68, v68
	v_exp_f32_e32 v69, v69
	v_exp_f32_e32 v70, v70
	v_exp_f32_e32 v71, v71
	v_mfma_f32_32x32x16_bf16 v[32:47], v[108:111], v[84:87], v[32:47]
	v_cvt_pk_bf16_f32 v80, v64, v65
	v_cvt_pk_bf16_f32 v81, v66, v67
	v_cvt_pk_bf16_f32 v82, v68, v69
	v_cvt_pk_bf16_f32 v83, v70, v71
	ds_read_b128 v[100:103], v128 offset:17408
	ds_read_b128 v[108:111], v128 offset:19456
	v_exp_f32_e32 v72, v72
	v_exp_f32_e32 v73, v73
	v_exp_f32_e32 v74, v74
	v_exp_f32_e32 v75, v75
	s_waitcnt lgkmcnt(7)
	v_mfma_f32_32x32x16_bf16 v[16:31], v[112:115], v[80:83], v[16:31]
	v_exp_f32_e32 v76, v76
	v_exp_f32_e32 v77, v77
	v_exp_f32_e32 v78, v78
	v_exp_f32_e32 v79, v79
	v_mfma_f32_32x32x16_bf16 v[32:47], v[120:123], v[80:83], v[32:47]
	v_cvt_pk_bf16_f32 v84, v72, v73
	v_cvt_pk_bf16_f32 v85, v74, v75
	v_cvt_pk_bf16_f32 v86, v76, v77
	v_cvt_pk_bf16_f32 v87, v78, v79
	s_waitcnt lgkmcnt(4)
	v_mfma_f32_32x32x16_f16 v[64:79], v[92:95], v[8:11], 0
	ds_read_b128 v[88:91], v129 offset:24576
	ds_read_b128 v[112:115], v128 offset:20480
	ds_read_b128 v[120:123], v128 offset:22528
	v_exp_f32_e32 v48, v48
	v_exp_f32_e32 v49, v49
	v_exp_f32_e32 v50, v50
	v_exp_f32_e32 v51, v51
	v_mfma_f32_32x32x16_bf16 v[16:31], v[116:119], v[84:87], v[16:31]
	v_exp_f32_e32 v52, v52
	v_exp_f32_e32 v53, v53
	v_exp_f32_e32 v54, v54
	v_exp_f32_e32 v55, v55
	v_mfma_f32_32x32x16_bf16 v[32:47], v[124:127], v[84:87], v[32:47]
	v_cvt_pk_bf16_f32 v80, v48, v49
	v_cvt_pk_bf16_f32 v81, v50, v51
	v_cvt_pk_bf16_f32 v82, v52, v53
	v_cvt_pk_bf16_f32 v83, v54, v55
	ds_read_b128 v[116:119], v128 offset:21504
	ds_read_b128 v[124:127], v128 offset:23552
	v_exp_f32_e32 v56, v56
	v_exp_f32_e32 v57, v57
	v_exp_f32_e32 v58, v58
	v_exp_f32_e32 v59, v59
	s_waitcnt lgkmcnt(7)
	v_mfma_f32_32x32x16_bf16 v[16:31], v[96:99], v[80:83], v[16:31]
	v_exp_f32_e32 v60, v60
	v_exp_f32_e32 v61, v61
	v_exp_f32_e32 v62, v62
	v_exp_f32_e32 v63, v63
	v_mfma_f32_32x32x16_bf16 v[32:47], v[104:107], v[80:83], v[32:47]
	v_cvt_pk_bf16_f32 v84, v56, v57
	v_cvt_pk_bf16_f32 v85, v58, v59
	v_cvt_pk_bf16_f32 v86, v60, v61
	v_cvt_pk_bf16_f32 v87, v62, v63
	s_waitcnt lgkmcnt(4)
	v_mfma_f32_32x32x16_f16 v[48:63], v[88:91], v[8:11], 0
	ds_read_b128 v[92:95], v129 offset:25600
	ds_read_b128 v[96:99], v129 offset:0
	ds_read_b128 v[104:107], v129 offset:2048
	v_exp_f32_e32 v64, v64
	v_exp_f32_e32 v65, v65
	v_exp_f32_e32 v66, v66
	v_exp_f32_e32 v67, v67
	v_mfma_f32_32x32x16_bf16 v[16:31], v[100:103], v[84:87], v[16:31]
	v_exp_f32_e32 v68, v68
	v_exp_f32_e32 v69, v69
	v_exp_f32_e32 v70, v70
	v_exp_f32_e32 v71, v71
	v_mfma_f32_32x32x16_bf16 v[32:47], v[108:111], v[84:87], v[32:47]
	v_cvt_pk_bf16_f32 v80, v64, v65
	v_cvt_pk_bf16_f32 v81, v66, v67
	v_cvt_pk_bf16_f32 v82, v68, v69
	v_cvt_pk_bf16_f32 v83, v70, v71
	ds_read_b128 v[100:103], v129 offset:1024
	ds_read_b128 v[108:111], v129 offset:3072
	v_exp_f32_e32 v72, v72
	v_exp_f32_e32 v73, v73
	v_exp_f32_e32 v74, v74
	v_exp_f32_e32 v75, v75
	s_waitcnt lgkmcnt(7)
	v_mfma_f32_32x32x16_bf16 v[16:31], v[112:115], v[80:83], v[16:31]
	v_exp_f32_e32 v76, v76
	v_exp_f32_e32 v77, v77
	v_exp_f32_e32 v78, v78
	v_exp_f32_e32 v79, v79
	v_mfma_f32_32x32x16_bf16 v[32:47], v[120:123], v[80:83], v[32:47]
	v_cvt_pk_bf16_f32 v84, v72, v73
	v_cvt_pk_bf16_f32 v85, v74, v75
	v_cvt_pk_bf16_f32 v86, v76, v77
	v_cvt_pk_bf16_f32 v87, v78, v79
	s_waitcnt lgkmcnt(5)
	s_nop 0
	v_mfma_f32_32x32x16_bf16 v[16:31], v[116:119], v[84:87], v[16:31]
	v_mfma_f32_32x32x16_bf16 v[32:47], v[124:127], v[84:87], v[32:47]
	s_mov_b32 s30, s46
	s_mov_b32 s46, s47
	s_mov_b32 s47, s48
	s_mov_b32 s48, s30
	s_add_u32 s27, s27, 1
	s_cmp_lt_u32 s27, 9
	s_cbranch_scc0 .Lm_flush
	s_cmp_eq_u32 s27, s25
	s_cbranch_scc1 .Lm_flush
	s_waitcnt vmcnt(0)
.Lm_bar:
	s_barrier
	v_add_u32_e32 v128, s46, v2
	v_add_u32_e32 v129, s47, v2
	s_add_u32 s28, s27, 2
	s_branch .Lm_steps

_Z11pam_combinePKDF16_PKfS2_S2_Pf:
	v_lshl_or_b32 v0, s2, 8, v0
	s_mov_b32 s2, 0x1f800
	v_cmp_gt_i32_e32 vcc, s2, v0
	s_and_saveexec_b64 s[2:3], vcc
	s_cbranch_execz .LBB2_3
	s_mov_b32 s2, 0x92492493
	v_mul_hi_i32 v1, v0, s2
	v_add_u32_e32 v1, v1, v0
	v_lshrrev_b32_e32 v2, 31, v1
	v_ashrrev_i32_e32 v1, 2, v1
	s_mov_b32 s2, 0x30c30c31
	v_add_u32_e32 v35, v1, v2
	v_mul_hi_i32 v1, v0, s2
	v_lshrrev_b32_e32 v2, 31, v1
	v_ashrrev_i32_e32 v1, 9, v1
	v_add_u32_e32 v1, v1, v2
	v_mul_i32_i24_e32 v2, 0x120, v1
	s_mov_b32 s3, 0x4bda12f7
	v_mul_hi_i32 v2, v2, s3
	s_movk_i32 s2, 0xfe80
	v_lshrrev_b32_e32 v3, 31, v2
	v_ashrrev_i32_e32 v2, 4, v2
	v_mad_i32_i24 v20, v1, s2, v35
	s_movk_i32 s2, 0x120
	v_add_u32_e32 v14, v2, v3
	v_mov_b32_e32 v2, 0x11f
	v_mad_i32_i24 v2, v1, s2, v2
	v_mul_hi_i32 v2, v2, s3
	v_lshrrev_b32_e32 v3, 31, v2
	v_ashrrev_i32_e32 v2, 4, v2
	v_add_u32_e32 v2, v2, v3
	v_sub_u32_e32 v34, v2, v14
	v_min_i32_e32 v2, 0, v34
	v_add_u32_e32 v2, v2, v14
	v_mul_lo_u32 v3, v2, 54
	s_mov_b32 s4, 0x38e38e39
	v_mul_hi_i32 v3, v3, s4
	v_lshrrev_b32_e32 v4, 31, v3
	v_ashrrev_i32_e32 v3, 6, v3
	v_add_u32_e32 v3, v3, v4
	v_min_i32_e32 v4, 1, v34
	v_add_u32_e32 v4, v4, v14
	v_mul_lo_u32 v5, v4, 54
	v_mul_hi_i32 v5, v5, s4
	v_lshrrev_b32_e32 v6, 31, v5
	v_ashrrev_i32_e32 v5, 6, v5
	v_add_u32_e32 v5, v5, v6
	v_min_i32_e32 v6, 2, v34
	v_add_u32_e32 v6, v6, v14
	v_mul_lo_u32 v7, v6, 54
	v_mul_hi_i32 v7, v7, s4
	v_lshrrev_b32_e32 v8, 31, v7
	v_ashrrev_i32_e32 v7, 6, v7
	v_add_u32_e32 v7, v7, v8
	v_min_i32_e32 v8, 3, v34
	v_add_u32_e32 v8, v8, v14
	v_mul_lo_u32 v9, v8, 54
	v_mul_hi_i32 v9, v9, s4
	v_lshrrev_b32_e32 v10, 31, v9
	v_ashrrev_i32_e32 v9, 6, v9
	v_add_u32_e32 v9, v9, v10
	v_min_i32_e32 v10, 4, v34
	v_add_u32_e32 v10, v10, v14
	v_mul_lo_u32 v11, v10, 54
	v_mul_hi_i32 v11, v11, s4
	v_lshrrev_b32_e32 v12, 31, v11
	v_ashrrev_i32_e32 v11, 6, v11
	v_add_u32_e32 v11, v11, v12
	v_min_i32_e32 v12, 5, v34
	v_add_u32_e32 v15, 0x100, v1
	v_cmp_eq_u32_e32 vcc, v3, v1
	v_add_u32_e32 v12, v12, v14
	v_mul_lo_u32 v13, v12, 54
	v_cndmask_b32_e32 v16, v15, v2, vcc
	v_cmp_eq_u32_e32 vcc, v5, v1
	v_mul_hi_i32 v13, v13, s4
	s_load_dwordx8 s[8:15], s[0:1], 0x0
	v_cndmask_b32_e32 v17, v15, v4, vcc
	v_cmp_eq_u32_e32 vcc, v7, v1
	v_lshrrev_b32_e32 v22, 31, v13
	v_ashrrev_i32_e32 v13, 6, v13
	v_cndmask_b32_e32 v18, v15, v6, vcc
	v_cmp_eq_u32_e32 vcc, v9, v1
	v_add_u32_e32 v13, v13, v22
	v_ashrrev_i32_e32 v21, 31, v20
	v_cndmask_b32_e32 v19, v15, v8, vcc
	v_cmp_eq_u32_e32 vcc, v11, v1
	s_movk_i32 s5, 0x180
	v_mad_u64_u32 v[4:5], s[2:3], v17, s5, v[20:21]
	v_cndmask_b32_e32 v26, v15, v10, vcc
	v_cmp_eq_u32_e32 vcc, v13, v1
	v_ashrrev_i32_e32 v5, 31, v4
	v_mad_u64_u32 v[6:7], s[2:3], v18, s5, v[20:21]
	v_cndmask_b32_e32 v30, v15, v12, vcc
	v_mad_u64_u32 v[8:9], s[2:3], v19, s5, v[20:21]
	v_mad_u64_u32 v[10:11], s[2:3], v26, s5, v[20:21]
	v_mad_u64_u32 v[12:13], s[2:3], v30, s5, v[20:21]
	s_waitcnt lgkmcnt(0)
	s_load_dword s18, s[14:15], 0x0
	v_mad_i32_i24 v68, v35, -7, v0
	v_mul_u32_u24_e32 v69, 0xc8, v35
	v_cmp_gt_i32_e32 vcc, 6, v68
	v_lshl_add_u32 v69, v68, 5, v69
	v_cndmask_b32_e64 v76, 0, 8, vcc
	global_load_dwordx2 v[70:71], v69, s[12:13]
	v_add_u32_e32 v77, v69, v76
	v_lshl_add_u32 v78, v76, 1, v69
	v_mad_u32_u24 v79, v76, 3, v69
	global_load_dwordx2 v[72:73], v77, s[12:13]
	global_load_dwordx2 v[74:75], v78, s[12:13]
	global_load_dwordx2 v[80:81], v79, s[12:13]
	v_lshl_add_u64 v[4:5], v[4:5], 2, s[10:11]
	v_ashrrev_i32_e32 v7, 31, v6
	v_ashrrev_i32_e32 v9, 31, v8
	v_ashrrev_i32_e32 v11, 31, v10
	v_ashrrev_i32_e32 v13, 31, v12
	v_lshl_add_u64 v[6:7], v[6:7], 2, s[10:11]
	v_lshl_add_u64 v[8:9], v[8:9], 2, s[10:11]
	v_lshl_add_u64 v[10:11], v[10:11], 2, s[10:11]
	v_lshl_add_u64 v[12:13], v[12:13], 2, s[10:11]
	global_load_dword v36, v[4:5], off
	global_load_dword v37, v[6:7], off
	global_load_dword v38, v[8:9], off
	global_load_dword v39, v[10:11], off
	global_load_dword v41, v[12:13], off
	v_min_i32_e32 v4, 6, v34
	v_add_u32_e32 v4, v4, v14
	v_mul_lo_u32 v5, v4, 54
	v_mul_hi_i32 v5, v5, s4
	v_lshrrev_b32_e32 v6, 31, v5
	v_ashrrev_i32_e32 v5, 6, v5
	v_add_u32_e32 v5, v5, v6
	v_cmp_eq_u32_e32 vcc, v5, v1
	v_mad_u64_u32 v[2:3], s[2:3], v16, s5, v[20:21]
	s_nop 0
	v_cndmask_b32_e32 v32, v15, v4, vcc
	v_mad_u64_u32 v[4:5], s[2:3], v32, s5, v[20:21]
	v_ashrrev_i32_e32 v5, 31, v4
	v_ashrrev_i32_e32 v3, 31, v2
	v_lshl_add_u64 v[4:5], v[4:5], 2, s[10:11]
	v_lshl_add_u64 v[2:3], v[2:3], 2, s[10:11]
	global_load_dword v43, v[4:5], off
	global_load_dword v40, v[2:3], off
	v_mad_u64_u32 v[44:45], s[2:3], v35, -7, v[0:1]
	v_lshlrev_b32_e32 v28, 3, v44
	v_ashrrev_i32_e32 v29, 31, v28
	v_lshl_add_u64 v[22:23], v[28:29], 1, s[8:9]
	v_mad_i64_i32 v[0:1], s[2:3], v16, s5, v[20:21]
	s_movk_i32 s4, 0x68
	v_mad_u64_u32 v[2:3], s[2:3], v0, s4, v[22:23]
	v_mad_i64_i32 v[4:5], s[2:3], v17, s5, v[20:21]
	v_mad_i32_i24 v3, v1, s4, v3
	v_mad_u64_u32 v[12:13], s[2:3], v4, s4, v[22:23]
	global_load_dwordx4 v[0:3], v[2:3], off nt
	v_mad_i32_i24 v13, v5, s4, v13
	v_mad_i64_i32 v[4:5], s[2:3], v18, s5, v[20:21]
	v_mad_u64_u32 v[14:15], s[2:3], v4, s4, v[22:23]
	v_mad_i32_i24 v15, v5, s4, v15
	global_load_dwordx4 v[4:7], v[12:13], off nt
	global_load_dwordx4 v[8:11], v[14:15], off nt
	v_mad_i64_i32 v[12:13], s[2:3], v19, s5, v[20:21]
	v_mad_u64_u32 v[24:25], s[2:3], v12, s4, v[22:23]
	v_mad_i32_i24 v25, v13, s4, v25
	v_mad_i64_i32 v[12:13], s[2:3], v26, s5, v[20:21]
	v_mad_u64_u32 v[26:27], s[2:3], v12, s4, v[22:23]
	v_mad_i32_i24 v27, v13, s4, v27
	global_load_dwordx4 v[12:15], v[24:25], off nt
	global_load_dwordx4 v[16:19], v[26:27], off nt
	v_mad_i64_i32 v[24:25], s[2:3], v30, s5, v[20:21]
	v_mad_u64_u32 v[30:31], s[2:3], v24, s4, v[22:23]
	v_mad_i64_i32 v[20:21], s[2:3], v32, s5, v[20:21]
	v_mad_i32_i24 v31, v25, s4, v31
	v_mad_u64_u32 v[32:33], s[2:3], v20, s4, v[22:23]
	v_mad_i32_i24 v33, v21, s4, v33
	global_load_dwordx4 v[20:23], v[30:31], off nt
	global_load_dwordx4 v[24:27], v[32:33], off nt
	s_movk_i32 s16, 0xc8
	v_mov_b64_e32 v[30:31], s[12:13]
	v_mad_i64_i32 v[30:31], s[2:3], v35, s16, v[30:31]
	v_lshlrev_b64 v[46:47], 2, v[28:29]
	v_lshl_add_u64 v[28:29], v[30:31], 0, v[46:47]
	v_mov_b32_e32 v30, 0xff61b1e6
	v_cmp_gt_i32_e32 vcc, 1, v34
	v_cmp_gt_i32_e64 s[2:3], 2, v34
	v_cmp_gt_i32_e64 s[4:5], 3, v34
	v_cmp_gt_i32_e64 s[6:7], 4, v34
	v_cmp_gt_i32_e64 s[8:9], 5, v34
	v_cmp_gt_i32_e64 s[10:11], 6, v34
	v_cmp_gt_i32_e64 s[12:13], 0, v34
	s_waitcnt vmcnt(13)
	v_cndmask_b32_e32 v31, v36, v30, vcc
	s_waitcnt vmcnt(12)
	v_cndmask_b32_e64 v32, v37, v30, s[2:3]
	s_waitcnt vmcnt(11)
	v_cndmask_b32_e64 v33, v38, v30, s[4:5]
	s_waitcnt vmcnt(10)
	v_cndmask_b32_e64 v42, v39, v30, s[6:7]
	s_waitcnt vmcnt(9)
	v_cndmask_b32_e64 v45, v41, v30, s[8:9]
	s_waitcnt vmcnt(8)
	v_cndmask_b32_e64 v50, v43, v30, s[10:11]
	s_waitcnt vmcnt(7)
	v_max_f32_e32 v48, v40, v40
	v_max_f32_e32 v51, 0xff61b1e6, v48
	v_cndmask_b32_e64 v30, v51, v30, s[12:13]
	v_max3_f32 v30, v30, v31, v32
	v_max3_f32 v30, v30, v33, v42
	v_max3_f32 v30, v30, v45, v50
	v_sub_f32_e32 v31, v40, v30
	v_exp_f32_e32 v31, v31
	v_sub_f32_e32 v32, v37, v30
	v_exp_f32_e32 v32, v32
	v_cndmask_b32_e64 v42, v31, 0, s[12:13]
	v_sub_f32_e32 v31, v36, v30
	v_exp_f32_e32 v31, v31
	v_cndmask_b32_e64 v34, v32, 0, s[2:3]
	v_sub_f32_e32 v32, v38, v30
	v_add_f32_e32 v33, 0, v42
	v_cndmask_b32_e64 v36, v31, 0, vcc
	v_exp_f32_e32 v32, v32
	v_add_f32_e32 v31, v33, v36
	v_sub_f32_e32 v33, v39, v30
	v_exp_f32_e32 v33, v33
	v_cndmask_b32_e64 v40, v32, 0, s[4:5]
	v_sub_f32_e32 v32, v41, v30
	v_exp_f32_e32 v32, v32
	v_sub_f32_e32 v30, v43, v30
	v_cndmask_b32_e64 v38, v33, 0, s[6:7]
	v_exp_f32_e32 v33, v30
	v_add_f32_e32 v31, v31, v34
	v_add_f32_e32 v31, v31, v40
	v_add_f32_e32 v31, v31, v38
	v_cndmask_b32_e64 v30, v32, 0, s[8:9]
	v_add_f32_e32 v31, v31, v30
	v_cndmask_b32_e64 v32, v33, 0, s[10:11]
	v_add_f32_e32 v31, v31, v32
	v_div_scale_f32 v33, s[2:3], v31, v31, 1.0
	v_rcp_f32_e32 v37, v33
	s_waitcnt vmcnt(6)
	v_cvt_f32_f16_e32 v56, v0
	v_cvt_f32_f16_sdwa v57, v0 dst_sel:DWORD dst_unused:UNUSED_PAD src0_sel:WORD_1
	s_waitcnt vmcnt(5)
	v_cvt_f32_f16_e32 v54, v4
	v_fma_f32 v39, -v33, v37, 1.0
	v_fmac_f32_e32 v37, v39, v37
	v_div_scale_f32 v39, vcc, 1.0, v31, 1.0
	v_cvt_f32_f16_sdwa v55, v4 dst_sel:DWORD dst_unused:UNUSED_PAD src0_sel:WORD_1
	s_load_dwordx2 s[4:5], s[0:1], 0x20
	v_mul_f32_e32 v41, v39, v37
	s_waitcnt vmcnt(4)
	v_cvt_f32_f16_e32 v58, v8
	v_cvt_f32_f16_sdwa v59, v8 dst_sel:DWORD dst_unused:UNUSED_PAD src0_sel:WORD_1
	v_fma_f32 v43, -v33, v41, v39
	v_pk_fma_f32 v[56:57], v[42:43], v[56:57], 0 op_sel_hi:[0,1,0]
	v_pk_fma_f32 v[54:55], v[36:37], v[54:55], v[56:57] op_sel_hi:[0,1,1]
	v_pk_fma_f32 v[54:55], v[34:35], v[58:59], v[54:55] op_sel_hi:[0,1,1]
	s_waitcnt vmcnt(3)
	v_cvt_f32_f16_e32 v58, v12
	v_cvt_f32_f16_sdwa v59, v12 dst_sel:DWORD dst_unused:UNUSED_PAD src0_sel:WORD_1
	s_waitcnt lgkmcnt(0)
	v_mov_b64_e32 v[50:51], s[4:5]
	s_waitcnt vmcnt(2)
	v_cvt_f32_f16_e32 v56, v16
	v_cvt_f32_f16_sdwa v57, v16 dst_sel:DWORD dst_unused:UNUSED_PAD src0_sel:WORD_1
	v_mad_i64_i32 v[50:51], s[4:5], v35, s16, v[50:51]
	s_waitcnt vmcnt(1)
	v_cvt_f32_f16_e32 v52, v20
	v_cvt_f32_f16_sdwa v53, v20 dst_sel:DWORD dst_unused:UNUSED_PAD src0_sel:WORD_1
	v_fmac_f32_e32 v41, v43, v37
	v_lshl_add_u64 v[46:47], v[50:51], 0, v[46:47]
	s_waitcnt vmcnt(0)
	v_cvt_f32_f16_e32 v50, v24
	v_cvt_f32_f16_sdwa v51, v24 dst_sel:DWORD dst_unused:UNUSED_PAD src0_sel:WORD_1
	v_pk_fma_f32 v[54:55], v[40:41], v[58:59], v[54:55] op_sel_hi:[0,1,1]
	v_fma_f32 v33, -v33, v41, v39
	v_pk_fma_f32 v[54:55], v[38:39], v[56:57], v[54:55] op_sel_hi:[0,1,1]
	v_div_fmas_f32 v33, v33, v37, v41
	v_pk_fma_f32 v[52:53], v[30:31], v[52:53], v[54:55] op_sel_hi:[0,1,1]
	v_cmp_gt_i32_e64 s[0:1], 6, v44
	v_div_fixup_f32 v44, v33, v31, 1.0
	v_pk_fma_f32 v[50:51], v[32:33], v[50:51], v[52:53] op_sel_hi:[0,1,1]
	v_pk_mul_f32 v[50:51], v[44:45], v[50:51] op_sel_hi:[0,1]
	s_waitcnt vmcnt(0) lgkmcnt(0)
	s_mov_b32 s19, s18
	v_pk_fma_f32 v[48:49], s[18:19], v[50:51], v[70:71] op_sel_hi:[0,1,1]
	global_store_dwordx2 v[46:47], v[48:49], off
	s_and_b64 exec, exec, s[0:1]
	s_cbranch_execz .LBB2_3
	v_cvt_f32_f16_sdwa v49, v25 dst_sel:DWORD dst_unused:UNUSED_PAD src0_sel:WORD_1
	v_cvt_f32_f16_e32 v48, v25
	v_cvt_f32_f16_sdwa v25, v21 dst_sel:DWORD dst_unused:UNUSED_PAD src0_sel:WORD_1
	v_cvt_f32_f16_e32 v24, v21
	v_cvt_f32_f16_sdwa v21, v17 dst_sel:DWORD dst_unused:UNUSED_PAD src0_sel:WORD_1
	v_cvt_f32_f16_e32 v20, v17
	v_cvt_f32_f16_sdwa v17, v13 dst_sel:DWORD dst_unused:UNUSED_PAD src0_sel:WORD_1
	v_cvt_f32_f16_e32 v16, v13
	v_cvt_f32_f16_sdwa v13, v26 dst_sel:DWORD dst_unused:UNUSED_PAD src0_sel:WORD_1
	v_cvt_f32_f16_e32 v12, v26
	v_cvt_f32_f16_sdwa v51, v27 dst_sel:DWORD dst_unused:UNUSED_PAD src0_sel:WORD_1
	v_cvt_f32_f16_e32 v50, v27
	v_cvt_f32_f16_sdwa v27, v22 dst_sel:DWORD dst_unused:UNUSED_PAD src0_sel:WORD_1
	v_cvt_f32_f16_e32 v26, v22
	v_cvt_f32_f16_sdwa v53, v23 dst_sel:DWORD dst_unused:UNUSED_PAD src0_sel:WORD_1
	v_cvt_f32_f16_e32 v52, v23
	v_cvt_f32_f16_sdwa v23, v18 dst_sel:DWORD dst_unused:UNUSED_PAD src0_sel:WORD_1
	v_cvt_f32_f16_e32 v22, v18
	v_cvt_f32_f16_sdwa v55, v19 dst_sel:DWORD dst_unused:UNUSED_PAD src0_sel:WORD_1
	v_cvt_f32_f16_e32 v54, v19
	v_cvt_f32_f16_sdwa v19, v14 dst_sel:DWORD dst_unused:UNUSED_PAD src0_sel:WORD_1
	v_cvt_f32_f16_e32 v18, v14
	v_cvt_f32_f16_sdwa v57, v15 dst_sel:DWORD dst_unused:UNUSED_PAD src0_sel:WORD_1
	v_cvt_f32_f16_e32 v56, v15
	v_cvt_f32_f16_sdwa v15, v9 dst_sel:DWORD dst_unused:UNUSED_PAD src0_sel:WORD_1
	v_cvt_f32_f16_e32 v14, v9
	v_cvt_f32_f16_sdwa v9, v10 dst_sel:DWORD dst_unused:UNUSED_PAD src0_sel:WORD_1
	v_cvt_f32_f16_e32 v8, v10
	v_cvt_f32_f16_sdwa v59, v11 dst_sel:DWORD dst_unused:UNUSED_PAD src0_sel:WORD_1
	v_cvt_f32_f16_e32 v58, v11
	v_cvt_f32_f16_sdwa v11, v5 dst_sel:DWORD dst_unused:UNUSED_PAD src0_sel:WORD_1
	v_cvt_f32_f16_e32 v10, v5
	v_cvt_f32_f16_sdwa v5, v6 dst_sel:DWORD dst_unused:UNUSED_PAD src0_sel:WORD_1
	v_cvt_f32_f16_e32 v4, v6
	v_cvt_f32_f16_sdwa v61, v7 dst_sel:DWORD dst_unused:UNUSED_PAD src0_sel:WORD_1
	v_cvt_f32_f16_e32 v60, v7
	v_cvt_f32_f16_sdwa v7, v1 dst_sel:DWORD dst_unused:UNUSED_PAD src0_sel:WORD_1
	v_cvt_f32_f16_e32 v6, v1
	v_cvt_f32_f16_sdwa v1, v2 dst_sel:DWORD dst_unused:UNUSED_PAD src0_sel:WORD_1
	v_cvt_f32_f16_e32 v0, v2
	v_cvt_f32_f16_sdwa v63, v3 dst_sel:DWORD dst_unused:UNUSED_PAD src0_sel:WORD_1
	v_cvt_f32_f16_e32 v62, v3
	v_cndmask_b32_e64 v2, 0, 8, s[0:1]
	v_mov_b32_e32 v3, 0
	v_lshl_add_u64 v[64:65], v[28:29], 0, v[2:3]
	v_cndmask_b32_e64 v2, 0, 16, s[0:1]
	v_mov_b32_e32 v43, v42
	v_lshl_add_u64 v[66:67], v[28:29], 0, v[2:3]
	v_cndmask_b32_e64 v2, 0, 24, s[0:1]
	v_mov_b32_e32 v37, v36
	v_pk_fma_f32 v[6:7], v[42:43], v[6:7], 0 op_sel_hi:[1,1,0]
	v_pk_fma_f32 v[0:1], v[42:43], v[0:1], 0 op_sel_hi:[1,1,0]
	v_lshl_add_u64 v[2:3], v[28:29], 0, v[2:3]
	v_pk_fma_f32 v[6:7], v[36:37], v[10:11], v[6:7]
	v_pk_fma_f32 v[0:1], v[36:37], v[4:5], v[0:1]
	v_pk_fma_f32 v[4:5], v[42:43], v[62:63], 0 op_sel_hi:[1,1,0]
	v_mov_b32_e32 v35, v34
	v_mov_b32_e32 v41, v40
	v_pk_fma_f32 v[2:3], v[36:37], v[60:61], v[4:5]
	v_pk_fma_f32 v[4:5], v[34:35], v[14:15], v[6:7]
	v_pk_fma_f32 v[0:1], v[34:35], v[8:9], v[0:1]
	v_mov_b32_e32 v39, v38
	v_pk_fma_f32 v[2:3], v[34:35], v[58:59], v[2:3]
	v_pk_fma_f32 v[4:5], v[40:41], v[16:17], v[4:5]
	v_pk_fma_f32 v[0:1], v[40:41], v[18:19], v[0:1]
	v_mov_b32_e32 v31, v30
	v_pk_fma_f32 v[2:3], v[40:41], v[56:57], v[2:3]
	v_pk_fma_f32 v[4:5], v[38:39], v[20:21], v[4:5]
	v_pk_fma_f32 v[0:1], v[38:39], v[22:23], v[0:1]
	v_mov_b32_e32 v33, v32
	v_pk_fma_f32 v[6:7], v[38:39], v[54:55], v[2:3]
	v_pk_fma_f32 v[2:3], v[30:31], v[24:25], v[4:5]
	v_pk_fma_f32 v[0:1], v[30:31], v[26:27], v[0:1]
	v_mov_b32_e32 v45, v44
	v_pk_fma_f32 v[2:3], v[32:33], v[48:49], v[2:3]
	v_pk_fma_f32 v[0:1], v[32:33], v[12:13], v[0:1]
	v_pk_mul_f32 v[2:3], v[44:45], v[2:3]
	v_pk_mul_f32 v[4:5], v[44:45], v[0:1]
	v_pk_fma_f32 v[0:1], s[18:19], v[2:3], v[72:73]
	v_pk_fma_f32 v[2:3], s[18:19], v[4:5], v[74:75]
	global_store_dwordx4 v[46:47], v[0:3], off offset:8
	s_nop 1
	v_pk_fma_f32 v[0:1], v[30:31], v[52:53], v[6:7]
	s_nop 0
	v_pk_fma_f32 v[0:1], v[32:33], v[50:51], v[0:1]
	s_nop 0
	v_pk_mul_f32 v[0:1], v[44:45], v[0:1]
	v_pk_fma_f32 v[0:1], s[18:19], v[0:1], v[80:81]
	global_store_dwordx2 v[46:47], v[0:1], off offset:24

	.amdhsa_kernel _Z11pam_combinePKDF16_PKfS2_S2_Pf
		.amdhsa_group_segment_fixed_size 0
		.amdhsa_private_segment_fixed_size 0
		.amdhsa_kernarg_size 40
		.amdhsa_user_sgpr_count 2
		.amdhsa_user_sgpr_dispatch_ptr 0
		.amdhsa_user_sgpr_queue_ptr 0
		.amdhsa_user_sgpr_kernarg_segment_ptr 1
		.amdhsa_user_sgpr_dispatch_id 0
		.amdhsa_user_sgpr_kernarg_preload_length 0
		.amdhsa_user_sgpr_kernarg_preload_offset 0
		.amdhsa_user_sgpr_private_segment_size 0
		.amdhsa_uses_dynamic_stack 0
		.amdhsa_enable_private_segment 0
		.amdhsa_system_sgpr_workgroup_id_x 1
		.amdhsa_system_sgpr_workgroup_id_y 0
		.amdhsa_system_sgpr_workgroup_id_z 0
		.amdhsa_system_sgpr_workgroup_info 0
		.amdhsa_system_vgpr_workitem_id 0
		.amdhsa_next_free_vgpr 84
		.amdhsa_next_free_sgpr 24
		.amdhsa_accum_offset 84
		.amdhsa_reserve_vcc 1
		.amdhsa_float_round_mode_32 0
		.amdhsa_float_round_mode_16_64 0
		.amdhsa_float_denorm_mode_32 3
		.amdhsa_float_denorm_mode_16_64 3
		.amdhsa_dx10_clamp 1
		.amdhsa_ieee_mode 1
		.amdhsa_fp16_overflow 0
		.amdhsa_tg_split 0
		.amdhsa_exception_fp_ieee_invalid_op 0
		.amdhsa_exception_fp_denorm_src 0
		.amdhsa_exception_fp_ieee_div_zero 0
		.amdhsa_exception_fp_ieee_overflow 0
		.amdhsa_exception_fp_ieee_underflow 0
		.amdhsa_exception_fp_ieee_inexact 0
		.amdhsa_exception_int_div_zero 0
	.end_amdhsa_kernel

amdhsa.kernels:
  - .agpr_count:     16
    .args:
      - .actual_access:  read_only
        .address_space:  global
        .offset:         0
        .size:           8
        .value_kind:     global_buffer
      - .actual_access:  read_only
        .address_space:  global
        .offset:         8
        .size:           8
        .value_kind:     global_buffer
      - .actual_access:  read_only
        .address_space:  global
        .offset:         16
        .size:           8
        .value_kind:     global_buffer
      - .actual_access:  read_only
        .address_space:  global
        .offset:         24
        .size:           8
        .value_kind:     global_buffer
      - .actual_access:  write_only
        .address_space:  global
        .offset:         32
        .size:           8
        .value_kind:     global_buffer
      - .actual_access:  write_only
        .address_space:  global
        .offset:         40
        .size:           8
        .value_kind:     global_buffer
      - .actual_access:  write_only
        .address_space:  global
        .offset:         48
        .size:           8
        .value_kind:     global_buffer
      - .actual_access:  write_only
        .address_space:  global
        .offset:         56
        .size:           8
        .value_kind:     global_buffer
      - .actual_access:  write_only
        .address_space:  global
        .offset:         64
        .size:           8
        .value_kind:     global_buffer
    .group_segment_fixed_size: 29184
    .kernarg_segment_align: 8
    .kernarg_segment_size: 72
    .language:       OpenCL C
    .language_version:
      - 2
      - 0
    .max_flat_workgroup_size: 256
    .name:           _Z8pam_prepPKfS0_S0_S0_PDv4_jS2_S2_PfS3_
    .private_segment_fixed_size: 0
    .sgpr_count:     28
    .sgpr_spill_count: 0
    .symbol:         _Z8pam_prepPKfS0_S0_S0_PDv4_jS2_S2_PfS3_.kd
    .uniform_work_group_size: 1
    .uses_dynamic_stack: false
    .vgpr_count:     52
    .vgpr_spill_count: 0
    .wavefront_size: 64
  - .agpr_count:     0
    .args:
      - .address_space:  global
        .offset:         0
        .size:           8
        .value_kind:     global_buffer
      - .actual_access:  read_only
        .address_space:  global
        .offset:         8
        .size:           8
        .value_kind:     global_buffer
      - .address_space:  global
        .offset:         16
        .size:           8
        .value_kind:     global_buffer
      - .actual_access:  read_only
        .address_space:  global
        .offset:         24
        .size:           8
        .value_kind:     global_buffer
      - .actual_access:  read_only
        .address_space:  global
        .offset:         32
        .size:           8
        .value_kind:     global_buffer
      - .actual_access:  write_only
        .address_space:  global
        .offset:         40
        .size:           8
        .value_kind:     global_buffer
      - .actual_access:  write_only
        .address_space:  global
        .offset:         48
        .size:           8
        .value_kind:     global_buffer
    .group_segment_fixed_size: 133120
    .kernarg_segment_align: 8
    .kernarg_segment_size: 56
    .language:       OpenCL C
    .language_version:
      - 2
      - 0
    .max_flat_workgroup_size: 768
    .name:           _Z8pam_mainPKDv4_jS1_S1_PKfS3_PDF16_Pf
    .private_segment_fixed_size: 0
    .sgpr_count:     52
    .sgpr_spill_count: 0
    .symbol:         _Z8pam_mainPKDv4_jS1_S1_PKfS3_PDF16_Pf.kd
    .uniform_work_group_size: 1
    .uses_dynamic_stack: false
    .vgpr_count:     152
    .vgpr_spill_count: 0
    .wavefront_size: 64
  - .agpr_count:     0
    .args:
      - .actual_access:  read_only
        .address_space:  global
        .offset:         0
        .size:           8
        .value_kind:     global_buffer
      - .actual_access:  read_only
        .address_space:  global
        .offset:         8
        .size:           8
        .value_kind:     global_buffer
      - .actual_access:  read_only
        .address_space:  global
        .offset:         16
        .size:           8
        .value_kind:     global_buffer
      - .actual_access:  read_only
        .address_space:  global
        .offset:         24
        .size:           8
        .value_kind:     global_buffer
      - .actual_access:  write_only
        .address_space:  global
        .offset:         32
        .size:           8
        .value_kind:     global_buffer
    .group_segment_fixed_size: 0
    .kernarg_segment_align: 8
    .kernarg_segment_size: 40
    .language:       OpenCL C
    .language_version:
      - 2
      - 0
    .max_flat_workgroup_size: 256
    .name:           _Z11pam_combinePKDF16_PKfS2_S2_Pf
    .private_segment_fixed_size: 0
    .sgpr_count:     30
    .sgpr_spill_count: 0
    .symbol:         _Z11pam_combinePKDF16_PKfS2_S2_Pf.kd
    .uniform_work_group_size: 1
    .uses_dynamic_stack: false
    .vgpr_count:     84
    .vgpr_spill_count: 0
    .wavefront_size: 64
